# MLA: one static s_setprio 1 for waves 4-7 before the step loop, per-segment s_setprio flips deleted (asm guide 7.4)
# baseline (speedup 1.0000x reference)
; #define LAS __attribute__((address_space(3)))
; #define GAS __attribute__((address_space(1)))
; __device__ __forceinline__ float ex2(float x) { return __builtin_amdgcn_exp2f(x); }
; __device__ __forceinline__ f32x16 mfma32(bf16x8 a, bf16x8 b, f32x16 c) { return __builtin_amdgcn_mfma_f32_32x32x16_bf16(a, b, c, 0, 0, 0); }
; #define MLA_WAITBAR() do { if (wid < 4) asm volatile("s_waitcnt vmcnt(6) lgkmcnt(0)\n\ts_barrier" ::: "memory"); else asm volatile("s_waitcnt vmcnt(4) lgkmcnt(0)\n\ts_barrier" ::: "memory"); } while (0)
; #define MLA_ISSUE(s) do { const int tk_ = (s) + 3 < NT - 1 ? (s) + 3 : NT - 1, tv_ = (s) + 2 < 0 ? 0 : ((s) + 2 < NT - 1 ? (s) + 2 : NT - 1); MLA_DMAK(tk_, ((s) + 3) & 3); MLA_DMAV(tv_, ((s) + 2) & 3); } while (0)
; #define PIN(x) asm volatile("" : "+v"(x))
; __device__ __forceinline__ void mla_unit(int b, int h, int qb, const bf16_t* __restrict__ Q, const bf16_t* __restrict__ KV, const bf16_t* __restrict__ PROJ, bf16_t* OCAT, float* SSQO, ldsp shm) {
;     ...
;     MLA_ISSUE(-3); MLA_ISSUE(-2); MLA_ISSUE(-1);
;     bf16x8 qr[6];
;     { const bf16_t* Qw = Q + (rowbase + q0 + wid * 32 + r32) * QW + h * 96 + hi * 8;
; #pragma unroll
;       for (int d0 = 0; d0 < 6; ++d0) qr[d0] = *(const GAS bf16x8*)(Qw + d0 * 16); }
;     asm volatile("s_waitcnt vmcnt(0)" ::: "memory");
;     LAS float* wsf = (LAS float*)(shm + WSF_OFF) + wid * 64;
;     const LAS unsigned char* vp0 = shm + VOFF + ((lane >> 4) & 1) * 32 + (lane & 3) * 8 + (4 * hi + ((lane & 15) >> 2)) * 64;
;     const LAS unsigned char* kp0 = shm + hi * 1024 + r32 * 16;
;     float mhat = 0.f, l_reg = 0.f; f32x16 o[2]; o[0] = f32x16{}; o[1] = f32x16{}; f32x16 negm = f32x16{};
;     f32x16 pA0, pA1, pB0, pB1;
;     ...
;     MLA_WAITBAR();
;     MLA_ISSUE(0);
;     { const LAS unsigned char* kb = kp0; pA0 = f32x16{}; pA1 = f32x16{};
; #pragma unroll
;       for (int d0 = 0; d0 < 6; ++d0) { const bf16x8 k0 = *(const LAS bf16x8*)(kb + d0 * 2048), k1 = *(const LAS bf16x8*)(kb + d0 * 2048 + 512); pA0 = mfma32(k0, qr[d0], pA0); pA1 = mfma32(k1, qr[d0], pA1); }
;       mhat = rowmax(pA0, pA1);
; #pragma unroll
;       for (int r = 0; r < 16; ++r) { negm[r] = -mhat; pA0[r] = ex2(pA0[r] - mhat); pA1[r] = ex2(pA1[r] - mhat); } }
;     PIN(negm);
.LBB0_1145:
	s_mov_b64 s[10:11], 0x40000
	v_lshlrev_b32_e32 v6, 10, v184
	v_lshlrev_b32_e32 v7, 4, v183
	v_lshl_add_u64 v[4:5], v[4:5], 0, s[10:11]
	s_add_i32 m0, s26, 0x10000
	v_add3_u32 v188, 0, v6, v7
	global_load_lds_dwordx4 v[4:5], off
	ds_read_b128 v[4:7], v188
	ds_read_b128 v[10:13], v188 offset:512
	s_waitcnt vmcnt(0) lgkmcnt(0)
	v_mfma_f32_32x32x16_bf16 v[20:35], v[4:7], v[136:139], 0
	v_lshlrev_b32_e32 v9, 8, v184
	s_and_b32 s8, s2, 0x3fffffc0
	s_lshl_b32 s8, s8, 2
	s_add_i32 s51, s8, 0
	s_mov_b32 s8, s9
	s_mov_b32 s10, s9
	s_mov_b32 s11, s9
	v_mfma_f32_32x32x16_bf16 v[52:67], v[10:13], v[136:139], 0
	ds_read_b128 v[4:7], v188 offset:2048
	ds_read_b128 v[10:13], v188 offset:2560
	s_mov_b32 s12, s9
	s_mov_b32 s13, s9
	s_mov_b32 s14, s9
	s_mov_b32 s15, s9
	s_mov_b32 s16, s9
	s_mov_b32 s17, s9
	s_waitcnt lgkmcnt(1)
	v_mfma_f32_32x32x16_bf16 v[20:35], v[4:7], v[132:135], v[20:35]
	s_mov_b32 s18, s9
	s_mov_b32 s19, s9
	s_mov_b32 s20, s9
	s_mov_b32 s21, s9
	s_mov_b32 s22, s9
	s_mov_b32 s23, s9
	s_lshl_b32 s3, s3, 2
	s_waitcnt lgkmcnt(0)
	v_mfma_f32_32x32x16_bf16 v[52:67], v[10:13], v[132:135], v[52:67]
	ds_read_b128 v[4:7], v188 offset:4096
	ds_read_b128 v[10:13], v188 offset:4608
	s_ashr_i32 s2, s2, 7
	s_add_i32 s51, s51, 0x14000
	s_add_i32 s52, s2, s3
	s_mov_b32 s27, 2
	s_add_i32 s52, s52, 1
	s_or_b32 s2, s3, 3
	s_waitcnt lgkmcnt(1)
	v_mfma_f32_32x32x16_bf16 v[20:35], v[4:7], v[128:131], v[20:35]
	ds_read_b128 v[4:7], v188 offset:6144
	ds_read_b128 v[36:39], v188 offset:10752
	v_cmp_gt_u32_e64 s[36:37], 32, v182
	v_lshl_add_u32 v185, v183, 2, s51
	v_mov_b32_e32 v189, 0
	s_waitcnt lgkmcnt(2)
	v_mfma_f32_32x32x16_bf16 v[52:67], v[10:13], v[128:131], v[52:67]
	ds_read_b128 v[10:13], v188 offset:6656
	s_waitcnt lgkmcnt(2)
	v_mfma_f32_32x32x16_bf16 v[20:35], v[4:7], v[124:127], v[20:35]
	v_lshlrev_b32_e32 v4, 1, v1
	v_and_b32_e32 v4, 32, v4
	v_add3_u32 v8, 0, v4, v8
	v_lshlrev_b32_e32 v4, 4, v1
	v_and_b32_e32 v14, 0xc0, v4
	ds_read_b128 v[4:7], v188 offset:8192
	v_add3_u32 v186, v8, v9, v14
	s_waitcnt lgkmcnt(1)
	v_mfma_f32_32x32x16_bf16 v[52:67], v[10:13], v[124:127], v[52:67]
	ds_read_b128 v[8:11], v188 offset:8704
	s_waitcnt lgkmcnt(1)
	v_mfma_f32_32x32x16_bf16 v[20:35], v[4:7], v[120:123], v[20:35]
	ds_read_b128 v[4:7], v188 offset:10240
	s_waitcnt lgkmcnt(1)
	v_mfma_f32_32x32x16_bf16 v[52:67], v[8:11], v[120:123], v[52:67]
	s_waitcnt lgkmcnt(0)
	v_mfma_f32_32x32x16_bf16 v[20:35], v[4:7], v[116:119], v[20:35]
	v_mov_b64_e32 v[4:5], s[8:9]
	v_mov_b64_e32 v[18:19], s[22:23]
	v_mov_b64_e32 v[6:7], s[10:11]
	v_mov_b64_e32 v[8:9], s[12:13]
	v_mov_b64_e32 v[10:11], s[14:15]
	v_mov_b64_e32 v[12:13], s[16:17]
	v_mov_b64_e32 v[14:15], s[18:19]
	v_mfma_f32_32x32x16_bf16 v[52:67], v[36:39], v[116:119], v[52:67]
	s_nop 3
	v_max_f32_e32 v40, v21, v21
	v_max_f32_e32 v41, v20, v20
	v_max_f32_e32 v40, v41, v40
	v_mov_b64_e32 v[16:17], s[20:21]
	s_mov_b32 s14, 0x8000
	s_nop 2
	v_max3_f32 v36, v22, v23, v53
	v_max3_f32 v37, v40, v52, v54
	v_max3_f32 v37, v37, v55, v24
	v_max3_f32 v36, v36, v26, v27
	v_max3_f32 v37, v37, v25, v56
	v_max3_f32 v36, v36, v58, v59
	v_max3_f32 v37, v37, v57, v28
	v_max3_f32 v36, v36, v30, v31
	v_max3_f32 v37, v37, v29, v60
	v_max3_f32 v36, v36, v62, v63
	v_max3_f32 v37, v37, v61, v32
	v_max3_f32 v36, v36, v34, v35
	v_max3_f32 v37, v37, v33, v64
	v_max3_f32 v36, v36, v66, v67
	v_max3_f32 v36, v37, v65, v36
	v_mov_b32_e32 v37, v36
	s_nop 1
	v_permlane32_swap_b32_e32 v36, v37
	v_max_f32_e32 v37, v37, v37
	v_max_f32_e32 v36, v36, v36
	v_max_f32_e32 v187, v36, v37
	v_sub_f32_e32 v20, v20, v187
	v_exp_f32_e32 v68, v20
	v_sub_f32_e32 v20, v21, v187
	v_exp_f32_e32 v69, v20
	v_sub_f32_e32 v20, v22, v187
	v_exp_f32_e32 v70, v20
	v_sub_f32_e32 v20, v23, v187
	v_exp_f32_e32 v71, v20
	v_sub_f32_e32 v20, v24, v187
	v_exp_f32_e32 v72, v20
	v_sub_f32_e32 v20, v25, v187
	v_exp_f32_e32 v73, v20
	v_sub_f32_e32 v20, v26, v187
	v_exp_f32_e32 v74, v20
	v_sub_f32_e32 v20, v27, v187
	v_exp_f32_e32 v75, v20
	v_sub_f32_e32 v20, v28, v187
	v_exp_f32_e32 v76, v20
	v_sub_f32_e32 v20, v29, v187
	v_exp_f32_e32 v77, v20
	v_sub_f32_e32 v20, v30, v187
	v_exp_f32_e32 v78, v20
	v_sub_f32_e32 v20, v31, v187
	v_exp_f32_e32 v79, v20
	v_sub_f32_e32 v20, v32, v187
	v_exp_f32_e32 v80, v20
	v_sub_f32_e32 v20, v33, v187
	v_exp_f32_e32 v81, v20
	v_sub_f32_e32 v20, v34, v187
	v_sub_f32_e32 v52, v52, v187
	v_sub_f32_e32 v53, v53, v187
	v_sub_f32_e32 v54, v54, v187
	v_sub_f32_e32 v55, v55, v187
	v_sub_f32_e32 v56, v56, v187
	v_sub_f32_e32 v57, v57, v187
	v_sub_f32_e32 v58, v58, v187
	v_sub_f32_e32 v59, v59, v187
	v_sub_f32_e32 v60, v60, v187
	v_sub_f32_e32 v61, v61, v187
	v_sub_f32_e32 v62, v62, v187
	v_sub_f32_e32 v63, v63, v187
	v_sub_f32_e32 v64, v64, v187
	v_sub_f32_e32 v65, v65, v187
	v_sub_f32_e32 v66, v66, v187
	v_sub_f32_e32 v67, v67, v187
	v_exp_f32_e32 v82, v20
	v_sub_f32_e32 v20, v35, v187
	v_exp_f32_e32 v52, v52
	v_exp_f32_e32 v53, v53
	v_exp_f32_e32 v54, v54
	v_exp_f32_e32 v55, v55
	v_exp_f32_e32 v56, v56
	v_exp_f32_e32 v57, v57
	v_exp_f32_e32 v58, v58
	v_exp_f32_e32 v59, v59
	v_exp_f32_e32 v83, v20
	v_xor_b32_e32 v36, 0x80000000, v187
	v_mov_b64_e32 v[34:35], v[18:19]
	v_mov_b32_e32 v37, v36
	v_mov_b32_e32 v38, v36
	v_mov_b32_e32 v39, v36
	v_mov_b32_e32 v40, v36
	v_mov_b32_e32 v41, v36
	v_mov_b32_e32 v42, v36
	v_mov_b32_e32 v43, v36
	v_mov_b32_e32 v44, v36
	v_mov_b32_e32 v45, v36
	v_mov_b32_e32 v46, v36
	v_mov_b32_e32 v47, v36
	v_mov_b32_e32 v48, v36
	v_mov_b32_e32 v49, v36
	v_mov_b32_e32 v50, v36
	v_mov_b32_e32 v51, v36
	v_mov_b64_e32 v[32:33], v[16:17]
	v_mov_b64_e32 v[30:31], v[14:15]
	v_mov_b64_e32 v[28:29], v[12:13]
	v_mov_b64_e32 v[26:27], v[10:11]
	v_mov_b64_e32 v[24:25], v[8:9]
	v_mov_b64_e32 v[22:23], v[6:7]
	v_mov_b64_e32 v[20:21], v[4:5]
	s_add_i32 s12, s27, -1
	s_and_b32 s12, s12, 3
	s_mulk_i32 s12, 0x3000
	v_add_u32_e32 v156, s12, v188
	s_and_b32 s12, s14, 0x6000
	v_add_u32_e32 v157, s12, v186
	s_and_b64 vcc, exec, s[40:41]
	s_cbranch_vccz .Lmla_prio_done
	s_setprio 1
; __device__ __forceinline__ void mla_unit(int b, int h, int qb, const bf16_t* __restrict__ Q, const bf16_t* __restrict__ KV, const bf16_t* __restrict__ PROJ, bf16_t* OCAT, float* SSQO, ldsp shm) {
;     ...
;     for (; t + 1 < NT; t += 2) { STEP(pB0, pB1, pA0, pA1, t); STEP(pA0, pA1, pB0, pB1, t + 1); }
.Lmla_prio_done:
.LBB0_1146:
.LBB0_1147:
	s_waitcnt vmcnt(4) lgkmcnt(0)
	s_barrier
.LBB0_1149:
	ds_read_b128 v[84:87], v156
	ds_read_b128 v[190:193], v156 offset:512
	ds_read_b128 v[194:197], v156 offset:2048
	ds_read_b128 v[198:201], v156 offset:2560
	s_waitcnt lgkmcnt(0)
	v_mfma_f32_32x32x16_bf16 v[100:115], v[84:87], v[136:139], v[36:51]
	s_add_i32 s19, s27, -1
	s_and_b32 s18, s19, 3
	s_mul_i32 s20, s18, 0x3000
	s_and_b32 s17, s14, 0x6000
	v_add_f32_e32 v88, v68, v69
	ds_read_b128 v[202:205], v156 offset:4096
	ds_read_b64_tr_b16 v[172:173], v157 offset:49152
	ds_read_b64_tr_b16 v[174:175], v157 offset:49664
	v_add_f32_e32 v84, v70, v88
	v_add_f32_e32 v84, v71, v84
	v_add_f32_e32 v84, v72, v84
	v_add_f32_e32 v144, v73, v84
	v_cvt_pk_bf16_f32 v140, v68, v69
	v_cvt_pk_bf16_f32 v141, v70, v71
	v_mfma_f32_32x32x16_bf16 v[84:99], v[190:193], v[136:139], v[36:51]
	ds_read_b128 v[190:193], v156 offset:4608
	ds_read_b64_tr_b16 v[68:69], v157 offset:53248
	ds_read_b64_tr_b16 v[70:71], v157 offset:53760
	v_add_f32_e32 v142, v74, v144
	v_add_f32_e32 v142, v75, v142
	v_add_f32_e32 v142, v76, v142
	v_add_f32_e32 v144, v77, v142
	v_cvt_pk_bf16_f32 v142, v72, v73
	v_cvt_pk_bf16_f32 v143, v74, v75
	v_mfma_f32_32x32x16_bf16 v[100:115], v[194:197], v[132:135], v[100:115]
	ds_read_b128 v[194:197], v156 offset:6144
	ds_read_b64_tr_b16 v[72:73], v157 offset:50176
	ds_read_b64_tr_b16 v[74:75], v157 offset:50688
	v_add_f32_e32 v144, v78, v144
	v_add_f32_e32 v144, v79, v144
	v_add_f32_e32 v144, v80, v144
	v_add_f32_e32 v148, v81, v144
	v_cvt_pk_bf16_f32 v144, v76, v77
	v_cvt_pk_bf16_f32 v145, v78, v79
	v_mfma_f32_32x32x16_bf16 v[84:99], v[198:201], v[132:135], v[84:99]
	ds_read_b128 v[198:201], v156 offset:6656
	ds_read_b64_tr_b16 v[76:77], v157 offset:54272
	ds_read_b64_tr_b16 v[78:79], v157 offset:54784
	v_add_f32_e32 v146, v82, v148
	v_add_f32_e32 v146, v83, v146
	v_add_f32_e32 v146, v52, v146
	v_add_f32_e32 v148, v53, v146
	v_cvt_pk_bf16_f32 v146, v80, v81
	v_cvt_pk_bf16_f32 v147, v82, v83
	v_exp_f32_e32 v60, v60
	v_exp_f32_e32 v61, v61
	v_exp_f32_e32 v62, v62
	v_exp_f32_e32 v63, v63
	s_waitcnt lgkmcnt(0)
	v_mfma_f32_32x32x16_bf16 v[100:115], v[202:205], v[128:131], v[100:115]
	ds_read_b128 v[202:205], v156 offset:8192
	ds_read_b64_tr_b16 v[80:81], v157 offset:51200
	ds_read_b64_tr_b16 v[82:83], v157 offset:51712
	v_add_f32_e32 v148, v54, v148
	v_add_f32_e32 v148, v55, v148
	v_add_f32_e32 v148, v56, v148
	v_add_f32_e32 v152, v57, v148
	v_cvt_pk_bf16_f32 v148, v52, v53
	v_cvt_pk_bf16_f32 v149, v54, v55
	v_exp_f32_e32 v64, v64
	v_exp_f32_e32 v65, v65
	v_exp_f32_e32 v66, v66
	v_exp_f32_e32 v67, v67
	v_mfma_f32_32x32x16_bf16 v[84:99], v[190:193], v[128:131], v[84:99]
	ds_read_b128 v[190:193], v156 offset:8704
	ds_read_b64_tr_b16 v[52:53], v157 offset:55296
	ds_read_b64_tr_b16 v[54:55], v157 offset:55808
	v_add_f32_e32 v150, v58, v152
	v_add_f32_e32 v150, v59, v150
	v_add_f32_e32 v150, v60, v150
	v_add_f32_e32 v152, v61, v150
	v_cvt_pk_bf16_f32 v150, v56, v57
	v_cvt_pk_bf16_f32 v151, v58, v59
	v_mfma_f32_32x32x16_bf16 v[100:115], v[194:197], v[124:127], v[100:115]
	ds_read_b128 v[194:197], v156 offset:10240
	ds_read_b64_tr_b16 v[56:57], v157 offset:52224
	ds_read_b64_tr_b16 v[58:59], v157 offset:52736
	v_add_f32_e32 v152, v62, v152
	v_add_f32_e32 v152, v63, v152
	v_add_f32_e32 v152, v64, v152
	v_add_f32_e32 v160, v65, v152
	v_cvt_pk_bf16_f32 v152, v60, v61
	v_cvt_pk_bf16_f32 v153, v62, v63
	v_mfma_f32_32x32x16_bf16 v[84:99], v[198:201], v[124:127], v[84:99]
	ds_read_b128 v[198:201], v156 offset:10752
	ds_read_b64_tr_b16 v[60:61], v157 offset:56320
	ds_read_b64_tr_b16 v[62:63], v157 offset:56832
	v_add_f32_e32 v154, v66, v160
	v_add_f32_e32 v156, v67, v154
	v_cvt_pk_bf16_f32 v154, v64, v65
	v_cvt_pk_bf16_f32 v155, v66, v67
	s_waitcnt lgkmcnt(0)
	v_mfma_f32_32x32x16_bf16 v[100:115], v[202:205], v[120:123], v[100:115]
	s_add_i32 s16, s27, 2
	s_min_i32 s8, s16, s2
	s_lshl_b64 s[10:11], s[8:9], 17
	v_lshl_add_u64 v[202:203], v[176:177], 0, s[10:11]
	s_and_b32 s10, s16, 3
	s_mulk_i32 s10, 0x3000
	s_add_i32 s10, s26, s10
	s_mov_b32 m0, s10
	s_nop 0
	global_load_lds_dwordx4 v[202:203], off
	v_mfma_f32_32x32x16_bf16 v[84:99], v[190:193], v[120:123], v[84:99]
	s_and_b64 vcc, exec, s[38:39]
	s_cbranch_vccnz .Lmla_rope1
	s_lshl_b64 s[12:13], s[8:9], 18
	v_lshl_add_u64 v[202:203], v[180:181], 0, s[12:13]
	s_add_i32 m0, s10, 0x2000
	s_nop 0
	global_load_lds_dwordx4 v[202:203], off
.Lmla_rope1:
	v_mfma_f32_32x32x16_bf16 v[100:115], v[194:197], v[116:119], v[100:115]
	s_add_i32 s8, s27, 1
	s_min_i32 s8, s8, s2
	s_lshl_b32 s8, s8, 17
	v_lshl_add_u64 v[202:203], v[178:179], 0, s[8:9]
	s_add_i32 s8, s14, 0xffffe000
	s_and_b32 s15, s8, 0x6000
	s_add_i32 s8, s26, s15
	v_lshl_add_u64 v[202:203], v[202:203], 0, s[24:25]
	s_add_i32 m0, s8, 0xc000
	s_nop 0
	global_load_lds_dwordx4 v[202:203], off
	v_mfma_f32_32x32x16_bf16 v[84:99], v[198:201], v[116:119], v[84:99]
	s_cmp_lt_i32 s19, s52
	s_cbranch_scc0 .LBB0_1167

; __device__ __forceinline__ void mla_unit(int b, int h, int qb, const bf16_t* __restrict__ Q, const bf16_t* __restrict__ KV, const bf16_t* __restrict__ PROJ, bf16_t* OCAT, float* SSQO, ldsp shm) {
;     ...
;     for (; t + 1 < NT; t += 2) { STEP(pB0, pB1, pA0, pA1, t); STEP(pA0, pA1, pB0, pB1, t + 1); }
.LBB0_1159:
	ds_read_b128 v[52:55], v140
	ds_read_b128 v[190:193], v140 offset:512
	ds_read_b128 v[194:197], v140 offset:2048
	ds_read_b128 v[198:201], v140 offset:2560
	s_waitcnt lgkmcnt(0)
	v_mfma_f32_32x32x16_bf16 v[68:83], v[52:55], v[136:139], v[36:51]
	v_add_f32_e32 v56, v100, v101
	ds_read_b128 v[202:205], v140 offset:4096
	ds_read_b64_tr_b16 v[172:173], v141 offset:49152
	ds_read_b64_tr_b16 v[174:175], v141 offset:49664
	v_add_f32_e32 v52, v102, v56
	v_add_f32_e32 v52, v103, v52
	v_add_f32_e32 v52, v104, v52
	v_add_f32_e32 v144, v105, v52
	v_cvt_pk_bf16_f32 v156, v100, v101
	v_cvt_pk_bf16_f32 v157, v102, v103
	v_mfma_f32_32x32x16_bf16 v[52:67], v[190:193], v[136:139], v[36:51]
	ds_read_b128 v[190:193], v140 offset:4608
	ds_read_b64_tr_b16 v[100:101], v141 offset:53248
	ds_read_b64_tr_b16 v[102:103], v141 offset:53760
	v_add_f32_e32 v144, v106, v144
	v_add_f32_e32 v144, v107, v144
	v_add_f32_e32 v144, v108, v144
	v_add_f32_e32 v144, v109, v144
	v_cvt_pk_bf16_f32 v158, v104, v105
	v_cvt_pk_bf16_f32 v159, v106, v107
	v_mfma_f32_32x32x16_bf16 v[68:83], v[194:197], v[132:135], v[68:83]
	ds_read_b128 v[194:197], v140 offset:6144
	ds_read_b64_tr_b16 v[104:105], v141 offset:50176
	ds_read_b64_tr_b16 v[106:107], v141 offset:50688
	v_add_f32_e32 v144, v110, v144
	v_add_f32_e32 v144, v111, v144
	v_add_f32_e32 v144, v112, v144
	v_add_f32_e32 v144, v113, v144
	v_cvt_pk_bf16_f32 v160, v108, v109
	v_cvt_pk_bf16_f32 v161, v110, v111
	v_mfma_f32_32x32x16_bf16 v[52:67], v[198:201], v[132:135], v[52:67]
	ds_read_b128 v[198:201], v140 offset:6656
	ds_read_b64_tr_b16 v[108:109], v141 offset:54272
	ds_read_b64_tr_b16 v[110:111], v141 offset:54784
	v_add_f32_e32 v144, v114, v144
	v_add_f32_e32 v144, v115, v144
	v_add_f32_e32 v144, v84, v144
	v_add_f32_e32 v144, v85, v144
	v_cvt_pk_bf16_f32 v162, v112, v113
	v_cvt_pk_bf16_f32 v163, v114, v115
	v_exp_f32_e32 v92, v92
	v_exp_f32_e32 v93, v93
	v_exp_f32_e32 v94, v94
	v_exp_f32_e32 v95, v95
	s_waitcnt lgkmcnt(0)
	v_mfma_f32_32x32x16_bf16 v[68:83], v[202:205], v[128:131], v[68:83]
	ds_read_b128 v[202:205], v140 offset:8192
	ds_read_b64_tr_b16 v[112:113], v141 offset:51200
	ds_read_b64_tr_b16 v[114:115], v141 offset:51712
	v_add_f32_e32 v144, v86, v144
	v_add_f32_e32 v144, v87, v144
	v_add_f32_e32 v144, v88, v144
	v_add_f32_e32 v144, v89, v144
	v_cvt_pk_bf16_f32 v164, v84, v85
	v_cvt_pk_bf16_f32 v165, v86, v87
	v_exp_f32_e32 v96, v96
	v_exp_f32_e32 v97, v97
	v_exp_f32_e32 v98, v98
	v_exp_f32_e32 v99, v99
	v_mfma_f32_32x32x16_bf16 v[52:67], v[190:193], v[128:131], v[52:67]
	ds_read_b128 v[190:193], v140 offset:8704
	ds_read_b64_tr_b16 v[84:85], v141 offset:55296
	ds_read_b64_tr_b16 v[86:87], v141 offset:55808
	v_add_f32_e32 v144, v90, v144
	v_add_f32_e32 v144, v91, v144
	v_add_f32_e32 v144, v92, v144
	v_add_f32_e32 v144, v93, v144
	v_cvt_pk_bf16_f32 v166, v88, v89
	v_cvt_pk_bf16_f32 v167, v90, v91
	v_mfma_f32_32x32x16_bf16 v[68:83], v[194:197], v[124:127], v[68:83]
	ds_read_b128 v[194:197], v140 offset:10240
	ds_read_b64_tr_b16 v[88:89], v141 offset:52224
	ds_read_b64_tr_b16 v[90:91], v141 offset:52736
	v_add_f32_e32 v144, v94, v144
	v_add_f32_e32 v144, v95, v144
	v_add_f32_e32 v144, v96, v144
	v_add_f32_e32 v144, v97, v144
	v_cvt_pk_bf16_f32 v168, v92, v93
	v_cvt_pk_bf16_f32 v169, v94, v95
	v_mfma_f32_32x32x16_bf16 v[52:67], v[198:201], v[124:127], v[52:67]
	ds_read_b128 v[198:201], v140 offset:10752
	ds_read_b64_tr_b16 v[92:93], v141 offset:56320
	ds_read_b64_tr_b16 v[94:95], v141 offset:56832
	v_add_f32_e32 v140, v98, v144
	v_add_f32_e32 v140, v99, v140
	v_cvt_pk_bf16_f32 v170, v96, v97
	v_cvt_pk_bf16_f32 v171, v98, v99
	s_waitcnt lgkmcnt(0)
	v_mfma_f32_32x32x16_bf16 v[68:83], v[202:205], v[120:123], v[68:83]
	s_add_i32 s8, s27, 3
	s_min_i32 s8, s8, s2
	s_lshl_b64 s[10:11], s[8:9], 17
	v_lshl_add_u64 v[202:203], v[176:177], 0, s[10:11]
	s_add_i32 s10, s26, s20
	s_mov_b32 m0, s10
	s_nop 0
	global_load_lds_dwordx4 v[202:203], off
	v_mfma_f32_32x32x16_bf16 v[52:67], v[190:193], v[120:123], v[52:67]
	s_and_b64 vcc, exec, s[38:39]
	s_cbranch_vccnz .Lmla_rope2
	s_lshl_b64 s[12:13], s[8:9], 18
	v_lshl_add_u64 v[202:203], v[180:181], 0, s[12:13]
	s_add_i32 m0, s10, 0x2000
	s_nop 0
	global_load_lds_dwordx4 v[202:203], off
.Lmla_rope2:
	v_mfma_f32_32x32x16_bf16 v[68:83], v[194:197], v[116:119], v[68:83]
	s_cmp_lt_u32 s19, s3
	s_cselect_b32 s8, s16, s2
	s_lshl_b64 s[10:11], s[8:9], 17
	v_lshl_add_u64 v[202:203], v[178:179], 0, s[10:11]
	s_add_i32 s8, s26, s17
	v_lshl_add_u64 v[202:203], v[202:203], 0, s[24:25]
	s_add_i32 m0, s8, 0xc000
	s_and_b32 s17, s27, 3
	global_load_lds_dwordx4 v[202:203], off
	s_mulk_i32 s17, 0x3000
	v_mfma_f32_32x32x16_bf16 v[52:67], v[198:201], v[116:119], v[52:67]
	s_cmp_lt_i32 s27, s52
	s_cbranch_scc0 .LBB0_1171

; __device__ __forceinline__ void mla_unit(int b, int h, int qb, const bf16_t* __restrict__ Q, const bf16_t* __restrict__ KV, const bf16_t* __restrict__ PROJ, bf16_t* OCAT, float* SSQO, ldsp shm) {
;     ...
;     STEP(pB0, pB1, pA0, pA1, t);
.LBB0_1181:
	s_xor_b32 s2, s15, 0x4000
	s_add_i32 s2, s2, 0
	v_lshl_add_u64 v[84:85], v[178:179], 0, s[8:9]
	s_add_i32 s2, s2, s34
	v_lshl_add_u64 v[84:85], v[84:85], 0, s[24:25]
	s_add_i32 m0, s2, 0xc000
	s_and_b32 s2, s12, 3
	global_load_lds_dwordx4 v[84:85], off
	s_mulk_i32 s2, 0x3000
	s_and_b32 s2, s14, 0x6000
	s_waitcnt lgkmcnt(0)
	v_mfma_f32_32x32x16_bf16 v[84:99], v[100:103], v[136:139], v[36:51]
	v_add_f32_e32 v144, v68, v69
	ds_read_b128 v[140:143], v156 offset:4096
	ds_read_b64_tr_b16 v[100:101], v157 offset:49152
	ds_read_b64_tr_b16 v[102:103], v157 offset:49664
	v_add_f32_e32 v144, v70, v144
	v_add_f32_e32 v144, v71, v144
	v_add_f32_e32 v144, v72, v144
	v_add_f32_e32 v144, v73, v144
	v_cvt_pk_bf16_f32 v68, v68, v69
	v_cvt_pk_bf16_f32 v69, v70, v71
	v_mfma_f32_32x32x16_bf16 v[36:51], v[104:107], v[136:139], v[36:51]
	ds_read_b128 v[136:139], v156 offset:4608
	ds_read_b64_tr_b16 v[104:105], v157 offset:53248
	ds_read_b64_tr_b16 v[106:107], v157 offset:53760
	v_add_f32_e32 v70, v74, v144
	v_add_f32_e32 v70, v75, v70
	v_add_f32_e32 v70, v76, v70
	v_add_f32_e32 v148, v77, v70
	v_cvt_pk_bf16_f32 v70, v72, v73
	v_cvt_pk_bf16_f32 v71, v74, v75
	v_mfma_f32_32x32x16_bf16 v[84:99], v[108:111], v[132:135], v[84:99]
	ds_read_b128 v[144:147], v156 offset:6144
	ds_read_b64_tr_b16 v[108:109], v157 offset:50176
	ds_read_b64_tr_b16 v[110:111], v157 offset:50688
	v_add_f32_e32 v72, v78, v148
	v_add_f32_e32 v72, v79, v72
	v_add_f32_e32 v72, v80, v72
	v_add_f32_e32 v152, v81, v72
	v_cvt_pk_bf16_f32 v72, v76, v77
	v_cvt_pk_bf16_f32 v73, v78, v79
	v_mfma_f32_32x32x16_bf16 v[36:51], v[112:115], v[132:135], v[36:51]
	ds_read_b128 v[148:151], v156 offset:6656
	ds_read_b64_tr_b16 v[76:77], v157 offset:54272
	ds_read_b64_tr_b16 v[78:79], v157 offset:54784
	v_add_f32_e32 v74, v82, v152
	v_add_f32_e32 v74, v83, v74
	v_add_f32_e32 v74, v52, v74
	v_add_f32_e32 v132, v53, v74
	v_cvt_pk_bf16_f32 v74, v80, v81
	v_cvt_pk_bf16_f32 v75, v82, v83
	v_exp_f32_e32 v60, v60
	v_exp_f32_e32 v61, v61
	v_exp_f32_e32 v62, v62
	v_exp_f32_e32 v63, v63
	s_waitcnt lgkmcnt(0)
	v_mfma_f32_32x32x16_bf16 v[84:99], v[140:143], v[128:131], v[84:99]
	ds_read_b128 v[140:143], v156 offset:8192
	ds_read_b64_tr_b16 v[112:113], v157 offset:51200
	ds_read_b64_tr_b16 v[114:115], v157 offset:51712
	v_add_f32_e32 v80, v54, v132
	v_add_f32_e32 v80, v55, v80
	v_add_f32_e32 v80, v56, v80
	v_add_f32_e32 v132, v57, v80
	v_cvt_pk_bf16_f32 v80, v52, v53
	v_cvt_pk_bf16_f32 v81, v54, v55
	v_exp_f32_e32 v64, v64
	v_exp_f32_e32 v65, v65
	v_exp_f32_e32 v66, v66
	v_exp_f32_e32 v67, v67
	v_mfma_f32_32x32x16_bf16 v[36:51], v[136:139], v[128:131], v[36:51]
	ds_read_b128 v[152:155], v156 offset:8704
	ds_read_b64_tr_b16 v[128:129], v157 offset:55296
	ds_read_b64_tr_b16 v[130:131], v157 offset:55808
	v_add_f32_e32 v52, v58, v132
	v_add_f32_e32 v52, v59, v52
	v_add_f32_e32 v52, v60, v52
	v_add_f32_e32 v52, v61, v52
	v_cvt_pk_bf16_f32 v82, v56, v57
	v_cvt_pk_bf16_f32 v83, v58, v59
	v_mfma_f32_32x32x16_bf16 v[84:99], v[144:147], v[124:127], v[84:99]
	ds_read_b128 v[54:57], v156 offset:10240
	ds_read_b64_tr_b16 v[136:137], v157 offset:52224
	ds_read_b64_tr_b16 v[138:139], v157 offset:52736
	v_add_f32_e32 v52, v62, v52
	v_add_f32_e32 v52, v63, v52
	v_add_f32_e32 v52, v64, v52
	v_add_f32_e32 v52, v65, v52
	v_cvt_pk_bf16_f32 v132, v60, v61
	v_cvt_pk_bf16_f32 v133, v62, v63
	v_mfma_f32_32x32x16_bf16 v[36:51], v[148:151], v[124:127], v[36:51]
	ds_read_b128 v[58:61], v156 offset:10752
	ds_read_b64_tr_b16 v[124:125], v157 offset:56320
	ds_read_b64_tr_b16 v[126:127], v157 offset:56832
	v_add_f32_e32 v52, v66, v52
	v_add_f32_e32 v52, v67, v52
	v_cvt_pk_bf16_f32 v134, v64, v65
	v_cvt_pk_bf16_f32 v135, v66, v67
	s_waitcnt lgkmcnt(0)
	v_mfma_f32_32x32x16_bf16 v[84:99], v[140:143], v[120:123], v[84:99]
	v_mfma_f32_32x32x16_bf16 v[36:51], v[152:155], v[120:123], v[36:51]
	v_mfma_f32_32x32x16_bf16 v[84:99], v[54:57], v[116:119], v[84:99]
	v_mfma_f32_32x32x16_bf16 v[36:51], v[58:61], v[116:119], v[36:51]
	s_cmp_lt_i32 s12, s52
	s_cbranch_scc0 .LBB0_1195

; __device__ __forceinline__ float rcpf_(float x) { return __builtin_amdgcn_rcpf(x); }
; __device__ __forceinline__ int crow(int r, int hi) { return (r & 3) + 8 * (r >> 2) + 4 * hi; }
; #define ATT_WAITBAR() asm volatile("s_waitcnt vmcnt(0) lgkmcnt(0)\n\ts_barrier" ::: "memory")
; __device__ __forceinline__ float swapsum(float m) { auto rr = __builtin_amdgcn_permlane32_swap(__float_as_uint(m), __float_as_uint(m), false, false); return __uint_as_float(rr[0]) + __uint_as_float(rr[1]); }
; __device__ __forceinline__ u32x4 packp(const f32x16& p, int b) { u32x4 w; w.x = cvt_pk_bf16(p[b], p[b + 1]); w.y = cvt_pk_bf16(p[b + 2], p[b + 3]); w.z = cvt_pk_bf16(p[b + 4], p[b + 5]); w.w = cvt_pk_bf16(p[b + 6], p[b + 7]); return w; }
; __device__ __forceinline__ void mla_unit(int b, int h, int qb, const bf16_t* __restrict__ Q, const bf16_t* __restrict__ KV, const bf16_t* __restrict__ PROJ, bf16_t* OCAT, float* SSQO, ldsp shm) {
;     ...
;     { float sacc = 0.f;
; #pragma unroll
;       for (int r = 0; r < 16; ++r) sacc += pB0[r] + pB1[r];
;       l_reg += sacc;
;       ATT_WAITBAR();
;       pv(o, vp0 + ((NT - 1) & 3) * VS, packp(pB0, 0), packp(pB0, 8), packp(pB1, 0), packp(pB1, 8)); }
;     ...
;     l_reg = swapsum(l_reg);
;     if (hi == 0) wsf[32 + r32] = l_reg;
;     asm volatile("s_waitcnt lgkmcnt(0)" ::: "memory");
;     float sc[16];
; #pragma unroll
;     for (int r = 0; r < 16; ++r) sc[r] = rcpf_(wsf[32 + crow(r, hi)]);
.LBB0_1185:
	s_setprio 0
	v_add_f32_e32 v52, v84, v36
	v_add_f32_e32 v52, 0, v52
	v_add_f32_e32 v54, v85, v37
	v_add_f32_e32 v52, v54, v52
	v_add_f32_e32 v54, v86, v38
	v_add_f32_e32 v52, v54, v52
	v_add_f32_e32 v54, v87, v39
	v_add_f32_e32 v52, v54, v52
	v_add_f32_e32 v54, v88, v40
	v_add_f32_e32 v52, v54, v52
	v_add_f32_e32 v54, v89, v41
	v_add_f32_e32 v52, v54, v52
	v_add_f32_e32 v54, v90, v42
	v_add_f32_e32 v52, v54, v52
	v_add_f32_e32 v54, v91, v43
	v_add_f32_e32 v52, v54, v52
	v_add_f32_e32 v54, v92, v44
	v_add_f32_e32 v52, v54, v52
	v_add_f32_e32 v54, v93, v45
	v_add_f32_e32 v52, v54, v52
	v_add_f32_e32 v54, v94, v46
	v_add_f32_e32 v52, v54, v52
	v_add_f32_e32 v54, v95, v47
	v_add_f32_e32 v52, v54, v52
	v_add_f32_e32 v54, v96, v48
	v_add_f32_e32 v52, v54, v52
	v_add_f32_e32 v54, v97, v49
	v_add_f32_e32 v52, v54, v52
	v_add_f32_e32 v54, v98, v50
	v_add_u32_e32 v53, 0xc000, v186
	v_add_f32_e32 v52, v54, v52
	v_add_f32_e32 v54, v99, v51
	v_add_f32_e32 v52, v54, v52
	s_waitcnt vmcnt(0) lgkmcnt(0)
	s_barrier
	v_cvt_pk_bf16_f32 v54, v84, v85
	v_cvt_pk_bf16_f32 v55, v86, v87
	v_cvt_pk_bf16_f32 v56, v88, v89
	v_cvt_pk_bf16_f32 v57, v90, v91
	v_cvt_pk_bf16_f32 v58, v92, v93
	v_cvt_pk_bf16_f32 v59, v94, v95
	v_cvt_pk_bf16_f32 v60, v96, v97
	v_cvt_pk_bf16_f32 v61, v98, v99
	v_cvt_pk_bf16_f32 v62, v36, v37
	v_cvt_pk_bf16_f32 v63, v38, v39
	v_cvt_pk_bf16_f32 v64, v40, v41
	v_cvt_pk_bf16_f32 v65, v42, v43
	v_cvt_pk_bf16_f32 v36, v44, v45
	v_cvt_pk_bf16_f32 v37, v46, v47
	v_cvt_pk_bf16_f32 v38, v48, v49
	v_cvt_pk_bf16_f32 v39, v50, v51
	ds_read_b64_tr_b16 v[40:41], v53 offset:24576
	ds_read_b64_tr_b16 v[42:43], v53 offset:25088
	ds_read_b64_tr_b16 v[44:45], v53 offset:25600
	ds_read_b64_tr_b16 v[46:47], v53 offset:26112
	ds_read_b64_tr_b16 v[48:49], v53 offset:26624
	ds_read_b64_tr_b16 v[50:51], v53 offset:27136
	ds_read_b64_tr_b16 v[66:67], v53 offset:27648
	ds_read_b64_tr_b16 v[68:69], v53 offset:28160
	s_waitcnt lgkmcnt(0)
	v_mfma_f32_32x32x16_bf16 v[4:19], v[54:57], v[40:43], v[4:19]
	v_add_f32_e32 v52, v116, v52
	v_mfma_f32_32x32x16_bf16 v[4:19], v[58:61], v[44:47], v[4:19]
	v_mfma_f32_32x32x16_bf16 v[4:19], v[62:65], v[48:51], v[4:19]
	v_mfma_f32_32x32x16_bf16 v[4:19], v[36:39], v[66:69], v[4:19]
	ds_read_b64_tr_b16 v[40:41], v53 offset:28672
	ds_read_b64_tr_b16 v[42:43], v53 offset:29184
	ds_read_b64_tr_b16 v[44:45], v53 offset:29696
	ds_read_b64_tr_b16 v[46:47], v53 offset:30208
	ds_read_b64_tr_b16 v[48:49], v53 offset:30720
	ds_read_b64_tr_b16 v[50:51], v53 offset:31232
	ds_read_b64_tr_b16 v[66:67], v53 offset:31744
	ds_read_b64_tr_b16 v[68:69], v53 offset:32256
	s_waitcnt lgkmcnt(0)
	v_mfma_f32_32x32x16_bf16 v[20:35], v[54:57], v[40:43], v[20:35]
	v_mfma_f32_32x32x16_bf16 v[20:35], v[58:61], v[44:47], v[20:35]
	v_mfma_f32_32x32x16_bf16 v[20:35], v[62:65], v[48:51], v[20:35]
	v_mfma_f32_32x32x16_bf16 v[20:35], v[36:39], v[66:69], v[20:35]
	v_mov_b32_e32 v36, v52
	s_nop 1
	v_permlane32_swap_b32_e32 v52, v36
	s_and_saveexec_b64 s[10:11], s[36:37]
	v_add_f32_e32 v36, v52, v36
	ds_write_b32 v185, v36 offset:128
	s_or_b64 exec, exec, s[10:11]
	s_waitcnt lgkmcnt(0)
	ds_read_b128 v[36:39], v2 offset:128
	ds_read_b128 v[40:43], v2 offset:160
	s_lshl_b64 s[2:3], s[30:31], 11
	s_add_u32 s2, s42, s2
	s_addc_u32 s3, s43, s3
	s_lshl_b32 s8, s49, 7
	s_add_u32 s12, s2, s8
	s_addc_u32 s13, s3, 0
	s_lshl_b64 s[2:3], s[30:31], 6
	s_waitcnt lgkmcnt(0)
	v_rcp_f32_e32 v44, v36
	v_rcp_f32_e32 v45, v37
	v_rcp_f32_e32 v46, v38
	v_rcp_f32_e32 v47, v39
	v_rcp_f32_e32 v48, v40
	ds_read_b128 v[36:39], v2 offset:192
	v_rcp_f32_e32 v49, v41
	v_rcp_f32_e32 v50, v42
	v_rcp_f32_e32 v51, v43
	ds_read_b128 v[40:43], v2 offset:224
	s_add_u32 s2, s44, s2
	s_addc_u32 s3, s45, s3
	s_lshl_b32 s8, s49, 2
	s_add_u32 s10, s2, s8
	s_addc_u32 s11, s3, 0
	s_lshl_b32 s2, s50, 12
	s_add_i32 s2, s2, 0
	s_waitcnt lgkmcnt(0)
; #define LAS __attribute__((address_space(3)))
; __device__ __forceinline__ unsigned cvt_pk_bf16(float lo, float hi) { unsigned r; asm volatile("v_cvt_pk_bf16_f32 %0, %1, %2" : "=v"(r) : "v"(lo), "v"(hi)); return r; }
; __device__ __forceinline__ float bf_lo(unsigned u) { return __uint_as_float(u << 16); }
; __device__ __forceinline__ float bf_hi(unsigned u) { return __uint_as_float(u & 0xffff0000u); }
; __device__ __forceinline__ float rcpf_(float x) { return __builtin_amdgcn_rcpf(x); }
; __device__ __forceinline__ int crow(int r, int hi) { return (r & 3) + 8 * (r >> 2) + 4 * hi; }
; __device__ __forceinline__ void store_o(const f32x16 (&o)[2], const float (&sc)[16], bf16_t* Ow, float* ssq  , ldsp stg, int lane, int r32, int hi) {
;     LAS bf16_t* s = (LAS bf16_t*)stg;
; #pragma unroll
;     for (int r = 0; r < 16; ++r) { const int orow = crow(r, hi);
; #pragma unroll
;         for (int d0 = 0; d0 < 2; ++d0) s[orow * 64 + d0 * 32 + r32] = (bf16_t)(cvt_pk_bf16(o[d0][r] * sc[r], 0.f) & 0xffffu); }
;     asm volatile("s_waitcnt lgkmcnt(0)" ::: "memory");
; #pragma unroll
;     for (int i = 0; i < 4; ++i) { const int row = i * 8 + (lane >> 3), ch = lane & 7; const u32x4 v = *(const LAS u32x4*)(s + row * 64 + ch * 8);
;         gst16(Ow + (size_t)row * 1024 + ch * 8, v);
;         float q = 0.f;
; #pragma unroll
;         for (int j = 0; j < 4; ++j) { const float a = bf_lo(v[j]), b = bf_hi(v[j]); q += a * a + b * b; }
;         q += __shfl_xor(q, 1); q += __shfl_xor(q, 2); q += __shfl_xor(q, 4);
;         if (ch == 0) ssq[(size_t)row * 16] = q; }
; }
; __device__ __forceinline__ void mla_unit(int b, int h, int qb, const bf16_t* __restrict__ Q, const bf16_t* __restrict__ KV, const bf16_t* __restrict__ PROJ, bf16_t* OCAT, float* SSQO, ldsp shm) {
;     ...
;     float sc[16];
; #pragma unroll
;     for (int r = 0; r < 16; ++r) sc[r] = rcpf_(wsf[32 + crow(r, hi)]);
;     const size_t row0 = rowbase + q0 + wid * 32;
;     store_o(o, sc, OCAT + row0 * 1024 + h * 64, SSQO + row0 * 16 + h, shm + OST_OFF + wid * 4096, lane, r32, hi);
	v_rcp_f32_e32 v2, v36
	v_rcp_f32_e32 v36, v37
	v_rcp_f32_e32 v37, v38
	v_rcp_f32_e32 v38, v39
	v_rcp_f32_e32 v39, v40
	v_rcp_f32_e32 v40, v41
	v_rcp_f32_e32 v41, v42
	v_rcp_f32_e32 v42, v43
	s_add_i32 s2, s2, 0x14800
	v_lshlrev_b32_e32 v43, 9, v184
	v_lshlrev_b32_e32 v52, 1, v183
	v_mul_f32_e32 v4, v4, v44
	v_add3_u32 v43, s2, v43, v52
	v_cvt_pk_bf16_f32 v4, v4, v3
	ds_write_b16 v43, v4
	v_mul_f32_e32 v4, v20, v44
	v_cvt_pk_bf16_f32 v4, v4, v3
	ds_write_b16 v43, v4 offset:64
	v_mul_f32_e32 v4, v5, v45
	v_cvt_pk_bf16_f32 v4, v4, v3
	ds_write_b16 v43, v4 offset:128
	v_mul_f32_e32 v4, v21, v45
	v_cvt_pk_bf16_f32 v4, v4, v3
	ds_write_b16 v43, v4 offset:192
	v_mul_f32_e32 v4, v6, v46
	v_cvt_pk_bf16_f32 v4, v4, v3
	ds_write_b16 v43, v4 offset:256
	v_mul_f32_e32 v4, v22, v46
	v_cvt_pk_bf16_f32 v4, v4, v3
	ds_write_b16 v43, v4 offset:320
	v_mul_f32_e32 v4, v7, v47
	v_cvt_pk_bf16_f32 v4, v4, v3
	ds_write_b16 v43, v4 offset:384
	v_mul_f32_e32 v4, v23, v47
	v_cvt_pk_bf16_f32 v4, v4, v3
	ds_write_b16 v43, v4 offset:448
	v_mul_f32_e32 v4, v8, v48
	v_cvt_pk_bf16_f32 v4, v4, v3
	ds_write_b16 v43, v4 offset:1024
	v_mul_f32_e32 v4, v24, v48
	v_cvt_pk_bf16_f32 v4, v4, v3
	ds_write_b16 v43, v4 offset:1088
	v_mul_f32_e32 v4, v9, v49
	v_cvt_pk_bf16_f32 v4, v4, v3
	ds_write_b16 v43, v4 offset:1152
	v_mul_f32_e32 v4, v25, v49
	v_cvt_pk_bf16_f32 v4, v4, v3
	ds_write_b16 v43, v4 offset:1216
	v_mul_f32_e32 v4, v10, v50
	v_cvt_pk_bf16_f32 v4, v4, v3
	ds_write_b16 v43, v4 offset:1280
	v_mul_f32_e32 v4, v26, v50
	v_cvt_pk_bf16_f32 v4, v4, v3
	ds_write_b16 v43, v4 offset:1344
	v_mul_f32_e32 v4, v11, v51
	v_cvt_pk_bf16_f32 v4, v4, v3
	ds_write_b16 v43, v4 offset:1408
	v_mul_f32_e32 v4, v27, v51
	v_cvt_pk_bf16_f32 v4, v4, v3
	ds_write_b16 v43, v4 offset:1472
	v_mul_f32_e32 v4, v12, v2
	v_mul_f32_e32 v2, v28, v2
	v_cvt_pk_bf16_f32 v4, v4, v3
	ds_write_b16 v43, v4 offset:2048
	v_cvt_pk_bf16_f32 v2, v2, v3
	ds_write_b16 v43, v2 offset:2112
	v_mul_f32_e32 v2, v13, v36
	v_cvt_pk_bf16_f32 v2, v2, v3
	ds_write_b16 v43, v2 offset:2176
	v_mul_f32_e32 v2, v29, v36
	v_cvt_pk_bf16_f32 v2, v2, v3
	ds_write_b16 v43, v2 offset:2240
	v_mul_f32_e32 v2, v14, v37
	v_cvt_pk_bf16_f32 v2, v2, v3
	ds_write_b16 v43, v2 offset:2304
	v_mul_f32_e32 v2, v30, v37
	v_cvt_pk_bf16_f32 v2, v2, v3
	ds_write_b16 v43, v2 offset:2368
	v_mul_f32_e32 v2, v15, v38
	v_cvt_pk_bf16_f32 v2, v2, v3
	ds_write_b16 v43, v2 offset:2432
	v_mul_f32_e32 v2, v31, v38
	v_cvt_pk_bf16_f32 v2, v2, v3
	ds_write_b16 v43, v2 offset:2496
	v_mul_f32_e32 v2, v16, v39
	v_cvt_pk_bf16_f32 v2, v2, v3
	ds_write_b16 v43, v2 offset:3072
	v_mul_f32_e32 v2, v32, v39
	v_cvt_pk_bf16_f32 v2, v2, v3
	ds_write_b16 v43, v2 offset:3136
	v_mul_f32_e32 v2, v17, v40
	v_cvt_pk_bf16_f32 v2, v2, v3
	ds_write_b16 v43, v2 offset:3200
	v_mul_f32_e32 v2, v33, v40
	v_cvt_pk_bf16_f32 v2, v2, v3
	ds_write_b16 v43, v2 offset:3264
	v_mul_f32_e32 v2, v18, v41
	v_cvt_pk_bf16_f32 v2, v2, v3
	ds_write_b16 v43, v2 offset:3328
	v_mul_f32_e32 v2, v34, v41
	v_cvt_pk_bf16_f32 v2, v2, v3
	ds_write_b16 v43, v2 offset:3392
	v_mul_f32_e32 v2, v19, v42
	v_cvt_pk_bf16_f32 v2, v2, v3
	ds_write_b16 v43, v2 offset:3456
	v_mul_f32_e32 v2, v35, v42
	v_cvt_pk_bf16_f32 v2, v2, v3
	v_and_b32_e32 v16, 7, v1
	ds_write_b16 v43, v2 offset:3520
	v_lshlrev_b32_e32 v2, 4, v16
	v_lshrrev_b32_e32 v7, 3, v182
	v_add_u32_e32 v8, s2, v2
	s_waitcnt lgkmcnt(0)
	v_lshl_add_u32 v6, v7, 7, v8
	ds_read_b128 v[12:15], v6
	v_lshl_add_u64 v[4:5], s[12:13], 0, v[2:3]
	v_and_b32_e32 v2, 64, v244
	v_xor_b32_e32 v1, 1, v244
	v_add_u32_e32 v2, 64, v2
	s_waitcnt lgkmcnt(0)
	v_and_b32_e32 v9, 0xffff0000, v12
	v_lshlrev_b32_e32 v6, 16, v12
	v_mul_f32_e32 v9, v9, v9
	v_and_b32_e32 v10, 0xffff0000, v13
	v_fmac_f32_e32 v9, v6, v6
	v_lshlrev_b32_e32 v6, 16, v13
	v_mul_f32_e32 v10, v10, v10
	v_fmac_f32_e32 v10, v6, v6
	v_add_f32_e32 v6, v9, v10
	v_and_b32_e32 v10, 0xffff0000, v14
	v_lshlrev_b32_e32 v9, 16, v14
	v_mul_f32_e32 v10, v10, v10
	v_fmac_f32_e32 v10, v9, v9
	v_add_f32_e32 v6, v10, v6
	v_and_b32_e32 v10, 0xffff0000, v15
	v_cmp_lt_i32_e32 vcc, v1, v2
	v_lshlrev_b32_e32 v9, 16, v15
	v_mul_f32_e32 v10, v10, v10
	v_cndmask_b32_e32 v1, v244, v1, vcc
	v_fmac_f32_e32 v10, v9, v9
	v_lshlrev_b32_e32 v1, 2, v1
	v_add_f32_e32 v9, v10, v6
	ds_bpermute_b32 v10, v1, v9
	v_xor_b32_e32 v6, 2, v244
	v_cmp_lt_i32_e32 vcc, v6, v2
	s_waitcnt lgkmcnt(0)
	v_add_f32_e32 v10, v9, v10
	v_cndmask_b32_e32 v6, v244, v6, vcc
	v_lshlrev_b32_e32 v6, 2, v6
	ds_bpermute_b32 v11, v6, v10
	v_xor_b32_e32 v9, 4, v244
	v_cmp_lt_i32_e32 vcc, v9, v2
	s_waitcnt lgkmcnt(0)
	v_add_f32_e32 v10, v10, v11
	v_cndmask_b32_e32 v2, v244, v9, vcc
	v_lshlrev_b32_e32 v9, 2, v2
	ds_bpermute_b32 v11, v9, v10
	v_lshlrev_b32_e32 v2, 11, v7
	v_cmp_eq_u32_e32 vcc, 0, v16
	v_lshl_add_u64 v[16:17], v[4:5], 0, v[2:3]
	global_store_dwordx4 v[16:17], v[12:15], off
	s_and_saveexec_b64 s[12:13], vcc
	v_readlane_b32 s26, v255, 34
	v_readlane_b32 s27, v255, 35
	s_cbranch_execz .LBB0_1189
	v_lshlrev_b32_e32 v2, 6, v7
	v_lshl_add_u64 v[12:13], s[10:11], 0, v[2:3]
	s_waitcnt lgkmcnt(0)
	v_add_f32_e32 v2, v10, v11
	flat_store_dword v[12:13], v2
